# speedup vs baseline: 1.0550x; 1.0021x over previous
.LBB0_5:
	s_or_b64 exec, exec, s[18:19]
	v_add_co_u32_e32 v6, vcc, 0x4000, v2
	s_mov_b32 s4, 0x8000
	s_nop 0
	v_addc_co_u32_e32 v7, vcc, 0, v3, vcc
	s_waitcnt lgkmcnt(0)
	s_barrier
	global_load_dword v42, v[2:3], off
	global_load_dword v43, v[6:7], off
	v_add_co_u32_e32 v6, vcc, s4, v2
	s_mov_b32 s4, 0xc000
	s_nop 0
	v_addc_co_u32_e32 v7, vcc, 0, v3, vcc
	v_add_co_u32_e32 v44, vcc, s4, v2
	s_mov_b32 s4, 0x10000
	s_nop 0
	v_addc_co_u32_e32 v45, vcc, 0, v3, vcc
	v_add_co_u32_e32 v46, vcc, s4, v2
	s_mov_b32 s4, 0x14000
	s_nop 0
	v_addc_co_u32_e32 v47, vcc, 0, v3, vcc
	v_lshlrev_b32_e32 v5, 2, v8
	v_add_co_u32_e32 v48, vcc, s4, v2
	global_load_dwordx4 v[10:13], v5, s[6:7] offset:48
	global_load_dwordx4 v[14:17], v5, s[8:9] offset:48
	global_load_dwordx4 v[18:21], v5, s[6:7] offset:32
	global_load_dwordx4 v[22:25], v5, s[8:9] offset:32
	global_load_dwordx4 v[26:29], v5, s[6:7] offset:16
	global_load_dwordx4 v[30:33], v5, s[8:9] offset:16
	global_load_dwordx4 v[34:37], v5, s[6:7]
	global_load_dwordx4 v[38:41], v5, s[8:9]
	v_addc_co_u32_e32 v49, vcc, 0, v3, vcc
	s_mov_b32 s4, 0x18000
	v_add_co_u32_e32 v50, vcc, s4, v2
	s_mov_b32 s4, 0x1c000
	s_nop 0
	v_addc_co_u32_e32 v51, vcc, 0, v3, vcc
	v_add_co_u32_e32 v52, vcc, s4, v2
	s_mov_b32 s4, 0x20000
	s_nop 0
	v_addc_co_u32_e32 v53, vcc, 0, v3, vcc
	v_add_co_u32_e32 v54, vcc, s4, v2
	s_mov_b32 s4, 0x24000
	s_nop 0
	v_addc_co_u32_e32 v55, vcc, 0, v3, vcc
	v_add_co_u32_e32 v56, vcc, s4, v2
	s_mov_b32 s4, 0x28000
	s_nop 0
	v_addc_co_u32_e32 v57, vcc, 0, v3, vcc
	global_load_dword v58, v[6:7], off
	global_load_dword v59, v[44:45], off
	global_load_dword v60, v[46:47], off
	global_load_dword v61, v[48:49], off
	global_load_dword v62, v[50:51], off
	global_load_dword v63, v[52:53], off
	global_load_dword v64, v[54:55], off
	global_load_dword v65, v[56:57], off
	v_add_co_u32_e32 v6, vcc, s4, v2
	s_mov_b32 s4, 0x2c000
	s_nop 0
	v_addc_co_u32_e32 v7, vcc, 0, v3, vcc
	v_add_co_u32_e32 v44, vcc, s4, v2
	s_mov_b32 s4, 0x30000
	s_nop 0
	v_addc_co_u32_e32 v45, vcc, 0, v3, vcc
	v_add_co_u32_e32 v46, vcc, s4, v2
	s_mov_b32 s4, 0x34000
	s_nop 0
	v_addc_co_u32_e32 v47, vcc, 0, v3, vcc
	v_add_co_u32_e32 v48, vcc, s4, v2
	s_mov_b32 s4, 0x38000
	s_nop 0
	v_addc_co_u32_e32 v49, vcc, 0, v3, vcc
	global_load_dword v50, v[6:7], off
	global_load_dword v51, v[44:45], off
	global_load_dword v52, v[46:47], off
	global_load_dword v53, v[48:49], off
	v_add_co_u32_e32 v6, vcc, s4, v2
	s_mov_b32 s4, 0x3c000
	s_nop 0
	v_addc_co_u32_e32 v7, vcc, 0, v3, vcc
	v_add_co_u32_e32 v44, vcc, s4, v2
	v_add_u32_e32 v4, 0x9000, v4
	s_nop 0
	v_addc_co_u32_e32 v45, vcc, 0, v3, vcc
	global_load_dword v46, v[6:7], off
	global_load_dword v47, v[44:45], off
	ds_read2_b32 v[6:7], v4 offset0:32 offset1:64
	v_lshlrev_b32_e32 v8, 1, v8
	s_movk_i32 s12, 0x404
	v_mad_u32_u24 v1, v1, s12, v8
	s_mov_b32 s4, 0x40000
	s_waitcnt lgkmcnt(0)
	v_mov_b32_e32 v4, v7
	s_waitcnt vmcnt(22)
	v_pk_add_f32 v[42:43], v[42:43], v[6:7] op_sel_hi:[1,0] neg_lo:[0,1] neg_hi:[0,1]
	s_nop 0
	v_pk_mul_f32 v[42:43], v[4:5], v[42:43] op_sel_hi:[0,1]
	s_waitcnt vmcnt(14)
	v_pk_fma_f32 v[34:35], v[34:35], v[42:43], v[38:39]
	s_nop 0
	v_cvt_pk_f16_f32 v7, v34, v35
	s_waitcnt vmcnt(12)
	v_pk_add_f32 v[8:9], v[58:59], v[6:7] op_sel_hi:[1,0] neg_lo:[0,1] neg_hi:[0,1]
	s_nop 0
	v_pk_mul_f32 v[8:9], v[4:5], v[8:9] op_sel_hi:[0,1]
	v_pk_fma_f32 v[8:9], v[36:37], v[8:9], v[40:41]
	s_nop 0
	v_cvt_pk_f16_f32 v8, v8, v9
	ds_write2_b32 v1, v7, v8 offset1:1
	s_waitcnt vmcnt(10)
	v_pk_add_f32 v[8:9], v[60:61], v[6:7] op_sel_hi:[1,0] neg_lo:[0,1] neg_hi:[0,1]
	s_nop 0
	v_pk_mul_f32 v[8:9], v[4:5], v[8:9] op_sel_hi:[0,1]
	v_pk_fma_f32 v[8:9], v[26:27], v[8:9], v[30:31]
	s_nop 0
	v_cvt_pk_f16_f32 v7, v8, v9
	s_waitcnt vmcnt(8)
	v_pk_add_f32 v[8:9], v[62:63], v[6:7] op_sel_hi:[1,0] neg_lo:[0,1] neg_hi:[0,1]
	s_nop 0
	v_pk_mul_f32 v[8:9], v[4:5], v[8:9] op_sel_hi:[0,1]
	v_pk_fma_f32 v[8:9], v[28:29], v[8:9], v[32:33]
	s_nop 0
	v_cvt_pk_f16_f32 v8, v8, v9
	ds_write2_b32 v1, v7, v8 offset0:2 offset1:3
	s_waitcnt vmcnt(6)
	v_pk_add_f32 v[8:9], v[64:65], v[6:7] op_sel_hi:[1,0] neg_lo:[0,1] neg_hi:[0,1]
	s_nop 0
	v_pk_mul_f32 v[8:9], v[4:5], v[8:9] op_sel_hi:[0,1]
	v_pk_fma_f32 v[8:9], v[18:19], v[8:9], v[22:23]
	s_nop 0
	v_cvt_pk_f16_f32 v7, v8, v9
	v_add_co_u32_e32 v8, vcc, s4, v2
	s_mov_b32 s4, 0x44000
	s_nop 0
	v_addc_co_u32_e32 v9, vcc, 0, v3, vcc
	v_add_co_u32_e32 v18, vcc, s4, v2
	s_mov_b32 s4, 0x48000
	s_nop 0
	v_addc_co_u32_e32 v19, vcc, 0, v3, vcc
	global_load_dword v40, v[8:9], off
	global_load_dword v41, v[18:19], off
	s_waitcnt vmcnt(6)
	v_pk_add_f32 v[8:9], v[50:51], v[6:7] op_sel_hi:[1,0] neg_lo:[0,1] neg_hi:[0,1]
	v_add_co_u32_e32 v32, vcc, s4, v2
	v_pk_mul_f32 v[8:9], v[4:5], v[8:9] op_sel_hi:[0,1]
	s_nop 0
	v_addc_co_u32_e32 v33, vcc, 0, v3, vcc
	s_mov_b32 s4, 0x4c000
	v_pk_fma_f32 v[8:9], v[20:21], v[8:9], v[24:25]
	v_add_co_u32_e32 v34, vcc, s4, v2
	v_cvt_pk_f16_f32 v8, v8, v9
	s_nop 0
	v_addc_co_u32_e32 v35, vcc, 0, v3, vcc
	s_mov_b32 s4, 0x50000
	ds_write2_b32 v1, v7, v8 offset0:4 offset1:5
	s_waitcnt vmcnt(4)
	v_pk_add_f32 v[8:9], v[52:53], v[6:7] op_sel_hi:[1,0] neg_lo:[0,1] neg_hi:[0,1]
	v_add_co_u32_e32 v36, vcc, s4, v2
	v_pk_mul_f32 v[8:9], v[4:5], v[8:9] op_sel_hi:[0,1]
	s_nop 0
	v_addc_co_u32_e32 v37, vcc, 0, v3, vcc
	s_mov_b32 s4, 0x54000
	v_pk_fma_f32 v[42:43], v[10:11], v[8:9], v[14:15]
	s_waitcnt vmcnt(2)
	v_pk_add_f32 v[8:9], v[46:47], v[6:7] op_sel_hi:[1,0] neg_lo:[0,1] neg_hi:[0,1]
	v_add_co_u32_e32 v38, vcc, s4, v2
	v_pk_mul_f32 v[8:9], v[4:5], v[8:9] op_sel_hi:[0,1]
	s_nop 0
	v_addc_co_u32_e32 v39, vcc, 0, v3, vcc
	s_mov_b32 s4, 0x58000
	v_pk_fma_f32 v[44:45], v[12:13], v[8:9], v[16:17]
	global_load_dwordx4 v[8:11], v5, s[6:7] offset:96
	global_load_dwordx4 v[12:15], v5, s[8:9] offset:96
	global_load_dwordx4 v[16:19], v5, s[6:7] offset:80
	global_load_dwordx4 v[20:23], v5, s[8:9] offset:80
	global_load_dwordx4 v[24:27], v5, s[6:7] offset:64
	global_load_dwordx4 v[28:31], v5, s[8:9] offset:64
	v_add_co_u32_e32 v46, vcc, s4, v2
	s_mov_b32 s4, 0x5c000
	s_nop 0
	v_addc_co_u32_e32 v47, vcc, 0, v3, vcc
	v_add_co_u32_e32 v48, vcc, s4, v2
	s_mov_b32 s4, 0x60000
	s_nop 0
	v_addc_co_u32_e32 v49, vcc, 0, v3, vcc
	v_add_co_u32_e32 v50, vcc, s4, v2
	s_mov_b32 s4, 0x64000
	s_nop 0
	v_addc_co_u32_e32 v51, vcc, 0, v3, vcc
	v_add_co_u32_e32 v52, vcc, s4, v2
	s_mov_b32 s4, 0x68000
	s_nop 0
	v_addc_co_u32_e32 v53, vcc, 0, v3, vcc
	global_load_dword v54, v[32:33], off
	global_load_dword v55, v[34:35], off
	global_load_dword v56, v[36:37], off
	global_load_dword v57, v[38:39], off
	global_load_dword v58, v[46:47], off
	global_load_dword v59, v[48:49], off
	global_load_dword v60, v[50:51], off
	global_load_dword v61, v[52:53], off
	v_add_co_u32_e32 v32, vcc, s4, v2
	s_mov_b32 s4, 0x6c000
	s_nop 0
	v_addc_co_u32_e32 v33, vcc, 0, v3, vcc
	v_add_co_u32_e32 v34, vcc, s4, v2
	s_mov_b32 s4, 0x70000
	s_nop 0
	v_addc_co_u32_e32 v35, vcc, 0, v3, vcc
	v_add_co_u32_e32 v48, vcc, s4, v2
	global_load_dword v46, v[32:33], off
	global_load_dword v47, v[34:35], off
	v_addc_co_u32_e32 v49, vcc, 0, v3, vcc
	s_mov_b32 s4, 0x74000
	v_add_co_u32_e32 v50, vcc, s4, v2
	s_mov_b32 s4, 0x78000
	s_nop 0
	v_addc_co_u32_e32 v51, vcc, 0, v3, vcc
	v_add_co_u32_e32 v52, vcc, s4, v2
	s_mov_b32 s4, 0x7c000
	s_nop 0
	v_addc_co_u32_e32 v53, vcc, 0, v3, vcc
	v_add_co_u32_e32 v2, vcc, s4, v2
	s_lshl_b64 s[4:5], s[16:17], 22
	s_nop 0
	v_addc_co_u32_e32 v3, vcc, 0, v3, vcc
	global_load_dword v62, v[48:49], off
	global_load_dword v63, v[50:51], off
	global_load_dword v64, v[52:53], off
	global_load_dword v65, v[2:3], off
	global_load_dwordx4 v[32:35], v5, s[6:7] offset:112
	global_load_dwordx4 v[36:39], v5, s[8:9] offset:112
	v_cvt_pk_f16_f32 v2, v42, v43
	v_cvt_pk_f16_f32 v3, v44, v45
	ds_write2_b32 v1, v2, v3 offset0:6 offset1:7
	s_waitcnt vmcnt(22)
	v_pk_add_f32 v[2:3], v[40:41], v[6:7] op_sel_hi:[1,0] neg_lo:[0,1] neg_hi:[0,1]
	s_add_u32 s4, s10, s4
	v_pk_mul_f32 v[2:3], v[4:5], v[2:3] op_sel_hi:[0,1]
	s_addc_u32 s5, s11, s5
	s_lshl_b32 s3, s3, 10
	s_add_u32 s4, s4, s3
	s_mov_b32 s6, 0
	s_mov_b32 s7, 1
	s_addc_u32 s5, s5, 0
	s_mov_b32 s3, 16
	s_waitcnt vmcnt(16)
	v_pk_fma_f32 v[2:3], v[24:25], v[2:3], v[28:29]
	s_nop 0
	v_cvt_pk_f16_f32 v5, v2, v3
	s_waitcnt vmcnt(14)
	v_pk_add_f32 v[2:3], v[54:55], v[6:7] op_sel_hi:[1,0] neg_lo:[0,1] neg_hi:[0,1]
	s_nop 0
	v_pk_mul_f32 v[2:3], v[4:5], v[2:3] op_sel_hi:[0,1]
	v_pk_fma_f32 v[2:3], v[26:27], v[2:3], v[30:31]
	s_nop 0
	v_cvt_pk_f16_f32 v2, v2, v3
	ds_write2_b32 v1, v5, v2 offset0:8 offset1:9
	s_waitcnt vmcnt(12)
	v_pk_add_f32 v[2:3], v[56:57], v[6:7] op_sel_hi:[1,0] neg_lo:[0,1] neg_hi:[0,1]
	s_nop 0
	v_pk_mul_f32 v[2:3], v[4:5], v[2:3] op_sel_hi:[0,1]
	v_pk_fma_f32 v[2:3], v[16:17], v[2:3], v[20:21]
	s_nop 0
	v_cvt_pk_f16_f32 v5, v2, v3
	s_waitcnt vmcnt(10)
	v_pk_add_f32 v[2:3], v[58:59], v[6:7] op_sel_hi:[1,0] neg_lo:[0,1] neg_hi:[0,1]
	s_nop 0
	v_pk_mul_f32 v[2:3], v[4:5], v[2:3] op_sel_hi:[0,1]
	v_pk_fma_f32 v[2:3], v[18:19], v[2:3], v[22:23]
	s_nop 0
	v_cvt_pk_f16_f32 v2, v2, v3
	ds_write2_b32 v1, v5, v2 offset0:10 offset1:11
	s_waitcnt vmcnt(8)
	v_pk_add_f32 v[2:3], v[60:61], v[6:7] op_sel_hi:[1,0] neg_lo:[0,1] neg_hi:[0,1]
	s_nop 0
	v_pk_mul_f32 v[2:3], v[4:5], v[2:3] op_sel_hi:[0,1]
	v_pk_fma_f32 v[2:3], v[8:9], v[2:3], v[12:13]
	v_or_b32_e32 v8, 0xc00, v0
	v_cvt_pk_f16_f32 v5, v2, v3
	s_waitcnt vmcnt(6)
	v_pk_add_f32 v[2:3], v[46:47], v[6:7] op_sel_hi:[1,0] neg_lo:[0,1] neg_hi:[0,1]
	v_mov_b32_e32 v9, v8
	v_pk_mul_f32 v[2:3], v[4:5], v[2:3] op_sel_hi:[0,1]
	v_pk_fma_f32 v[2:3], v[10:11], v[2:3], v[14:15]
	s_nop 0
	v_cvt_pk_f16_f32 v2, v2, v3
	ds_write2_b32 v1, v5, v2 offset0:12 offset1:13
	s_waitcnt vmcnt(4)
	v_pk_add_f32 v[2:3], v[62:63], v[6:7] op_sel_hi:[1,0] neg_lo:[0,1] neg_hi:[0,1]
	s_nop 0
	v_pk_mul_f32 v[2:3], v[4:5], v[2:3] op_sel_hi:[0,1]
	s_waitcnt vmcnt(0)
	v_pk_fma_f32 v[2:3], v[32:33], v[2:3], v[36:37]
	s_nop 0
	v_cvt_pk_f16_f32 v5, v2, v3
	v_pk_add_f32 v[2:3], v[64:65], v[6:7] op_sel_hi:[1,0] neg_lo:[0,1] neg_hi:[0,1]
	v_or_b32_e32 v6, 0x800, v0
	v_pk_mul_f32 v[2:3], v[4:5], v[2:3] op_sel_hi:[0,1]
	v_pk_fma_f32 v[2:3], v[34:35], v[2:3], v[38:39]
	v_or_b32_e32 v4, 0x400, v0
	v_cvt_pk_f16_f32 v2, v2, v3
	ds_write2_b32 v1, v5, v2 offset0:14 offset1:15
	v_and_b32_e32 v2, 0xff, v0
	v_lshlrev_b32_e32 v10, 2, v2
	v_mov_b32_e32 v1, v2
	v_mov_b32_e32 v3, v0
	v_mov_b32_e32 v5, v4
	v_mov_b32_e32 v7, v6
	s_waitcnt lgkmcnt(0)
	s_barrier
	v_lshrrev_b32_e32 v1, 6, v0
	v_and_b32_e32 v2, 63, v0
	v_mul_u32_u24_e32 v1, 0x404, v1
	v_lshl_add_u32 v1, v2, 4, v1
	v_lshlrev_b32_e32 v3, 4, v0
	ds_read2_b32 v[4:5], v1 offset1:1
	ds_read2_b32 v[6:7], v1 offset0:2 offset1:3
	v_add_u32_e32 v1, 0x2020, v1
	ds_read2_b32 v[8:9], v1 offset1:1
	ds_read2_b32 v[10:11], v1 offset0:2 offset1:3
	v_add_u32_e32 v1, 0x2020, v1
	ds_read2_b32 v[12:13], v1 offset1:1
	ds_read2_b32 v[14:15], v1 offset0:2 offset1:3
	v_add_u32_e32 v1, 0x2020, v1
	ds_read2_b32 v[16:17], v1 offset1:1
	ds_read2_b32 v[18:19], v1 offset0:2 offset1:3
	s_waitcnt lgkmcnt(6)
	global_store_dwordx4 v3, v[4:7], s[4:5] sc1
	v_add_u32_e32 v3, 0x2000, v3
	s_waitcnt lgkmcnt(4)
	global_store_dwordx4 v3, v[8:11], s[4:5] sc1
	v_add_u32_e32 v3, 0x2000, v3
	s_waitcnt lgkmcnt(2)
	global_store_dwordx4 v3, v[12:15], s[4:5] sc1
	v_add_u32_e32 v3, 0x2000, v3
	s_waitcnt lgkmcnt(0)
	global_store_dwordx4 v3, v[16:19], s[4:5] sc1
	s_mov_b64 s[4:5], 0
